# swa unit: all K/V tiles of the unit loaded in one batch and kept resident in LDS (6 slots), no per-tile global round trip
# baseline (speedup 1.0000x reference)
; __device__ __forceinline__ float bflo(unsigned w) { return __uint_as_float(w << 16); }
; __device__ __forceinline__ float bfhi(unsigned w) { return __uint_as_float(w & 0xFFFF0000u); }
; __device__ __forceinline__ unsigned pkbf(float lo, float hi) { f32x2_t v = {lo, hi}; bf16x2_t b = __builtin_convertvector(v, bf16x2_t); return __builtin_bit_cast(unsigned, b); }
;     ...
;         const int qi = 32 - u / 16, bk = u % 16, b = bk >> 1, hkv = bk & 1, hq = 2 * hkv + (wave >> 2);
;         const int q0 = qi == 0 ? 0 : 16 + 128 * (qi - 1);
;         const int ktlo = max(1, (q0 - 127) / 64), kthi = qi == 0 ? 0 : (q0 + 127) / 64;
;         const int ntile = 1 + (kthi >= ktlo ? kthi - ktlo + 1 : 0);
;         const int q0w = q0 + 32 * (wave & 3), qpos = q0w + l31;
;         const bool wave_on = (qi > 0) || ((wave & 3) == 0);
;         const size_t qrow = (size_t)b * LT + (qpos < LT ? qpos : LT - 1);
;         bf16x8 Qf[4]; bf16x8 qx; float lsum;
;         { u32x4 qraw[4]; float qn2 = 0.f;
; #pragma unroll
;           for (int s = 0; s < 4; ++s) qraw[s] = *(const u32x4*)(U + qrow * INW + C_QA + hq * 64 + s * 16 + hi * 8);
;           const float km2 = __uint_as_float(__hip_atomic_load((const unsigned*)(ws + WS_CTL) + CW_KMX + l * 256 + 128 + b * 2 + hkv, __ATOMIC_RELAXED, __HIP_MEMORY_SCOPE_AGENT));
; #pragma unroll
;           for (int s = 0; s < 4; ++s) { const unsigned qw[4] = {qraw[s].x, qraw[s].y, qraw[s].z, qraw[s].w}; u32x4 qs;
; #pragma unroll
;               for (int e = 0; e < 4; ++e) qn2 += bflo(qw[e]) * bflo(qw[e]) + bfhi(qw[e]) * bfhi(qw[e]);
;               qs.x = pkbf(bflo(qw[0]) * c2, bfhi(qw[0]) * c2); qs.y = pkbf(bflo(qw[1]) * c2, bfhi(qw[1]) * c2); qs.z = pkbf(bflo(qw[2]) * c2, bfhi(qw[2]) * c2); qs.w = pkbf(bflo(qw[3]) * c2, bfhi(qw[3]) * c2);
;               Qf[s] = __builtin_bit_cast(bf16x8, qs); }
;           qn2 += __shfl_xor(qn2, 32);
.LBB0_814:
	v_add_u32_e32 v2, v0, v2
	v_and_b32_e32 v2, -16, v2
	v_sub_u32_e32 v8, v0, v2
	v_and_b32_e32 v11, 1, v8
	v_lshlrev_b32_e32 v2, 1, v11
	s_waitcnt vmcnt(0)
	v_add_u32_e32 v76, s34, v2
	v_add_u32_e32 v2, 0xffffff81, v50
	v_ashrrev_i32_e32 v3, 31, v2
	v_lshrrev_b32_e32 v3, 26, v3
	v_add_u32_e32 v2, v2, v3
	v_ashrrev_i32_e32 v2, 6, v2
	v_max_i32_e32 v51, 1, v2
	v_add_u32_e32 v2, 0x7f, v50
	v_lshrrev_b32_e32 v2, 6, v2
	v_cndmask_b32_e64 v2, v2, 0, s[0:1]
	v_sub_co_u32_e32 v2, vcc, v2, v51
	v_lshrrev_b32_e32 v41, 1, v8
	v_readfirstlane_b32 s0, v2
	v_add_u32_e32 v120, s35, v50
	s_add_i32 s8, s0, 2
	v_add_u32_e32 v40, v120, v112
	s_movk_i32 s0, 0x200
	v_mul_lo_u32 v104, v41, s33
	v_cmp_gt_i32_e64 s[6:7], s0, v0
	v_ashrrev_i32_e32 v105, 31, v104
	v_min_i32_e32 v0, 0x100f, v40
	v_lshl_add_u64 v[2:3], v[0:1], 0, v[104:105]
	v_mov_b64_e32 v[4:5], s[16:17]
	v_mad_u64_u32 v[4:5], s[0:1], v2, s97, v[4:5]
	s_waitcnt vmcnt(0)
	v_lshlrev_b32_e32 v106, 6, v76
	v_mad_i32_i24 v5, v3, s97, v5
	v_ashrrev_i32_e32 v107, 31, v106
	v_lshl_add_u64 v[2:3], v[106:107], 1, v[4:5]
	v_mov_b32_e32 v103, v1
	v_lshl_add_u64 v[6:7], v[2:3], 0, v[102:103]
	global_load_dwordx4 v[2:5], v[6:7], off
	global_load_dwordx4 v[12:15], v[6:7], off offset:32
	global_load_dwordx4 v[42:45], v[6:7], off offset:64
	global_load_dwordx4 v[46:49], v[6:7], off offset:96
	v_and_b32_e32 v6, -2, v8
	v_ashrrev_i32_e32 v7, 31, v6
	v_lshlrev_b64 v[6:7], 2, v[6:7]
	s_and_b64 s[0:1], vcc, exec
	v_lshl_add_u64 v[6:7], s[26:27], 0, v[6:7]
	v_lshlrev_b32_e32 v0, 2, v11
	v_readfirstlane_b32 s1, v7
	v_readfirstlane_b32 s0, v6
	v_readlane_b32 s48, v253, 12
	v_readlane_b32 s58, v253, 22
	v_readlane_b32 s59, v253, 23
	s_cselect_b32 s37, 1, s8
	s_or_b64 s[28:29], s[6:7], s[24:25]
	global_load_dword v0, v0, s[0:1] sc1
	s_mov_b32 s0, 0xf800000
	s_cmp_lt_i32 s37, 1
	v_readlane_b32 s49, v253, 13
	v_readlane_b32 s50, v253, 14
	v_readlane_b32 s51, v253, 15
	v_readlane_b32 s52, v253, 16
	v_readlane_b32 s53, v253, 17
	v_readlane_b32 s54, v253, 18
	v_readlane_b32 s55, v253, 19
	v_readlane_b32 s56, v253, 20
	v_readlane_b32 s57, v253, 21
	v_readlane_b32 s60, v253, 24
	v_readlane_b32 s61, v253, 25
	v_readlane_b32 s62, v253, 26
	v_readlane_b32 s63, v253, 27
	s_waitcnt vmcnt(4)
	v_lshlrev_b32_e32 v20, 16, v2
	v_and_b32_e32 v21, 0xffff0000, v2
	v_lshlrev_b32_e32 v26, 16, v3
	s_waitcnt vmcnt(1)
	v_and_b32_e32 v7, 0xffff0000, v47
	v_and_b32_e32 v27, 0xffff0000, v3
	v_lshlrev_b32_e32 v30, 16, v14
	v_and_b32_e32 v31, 0xffff0000, v14
	v_lshlrev_b32_e32 v36, 16, v15
	v_and_b32_e32 v37, 0xffff0000, v15
	v_lshlrev_b32_e32 v10, 16, v46
	v_and_b32_e32 v15, 0xffff0000, v46
	v_mov_b32_e32 v14, v7
	v_and_b32_e32 v9, 0xffff0000, v49
	v_pk_mul_f32 v[52:53], v[20:21], v[20:21]
	v_pk_mul_f32 v[54:55], v[26:27], v[26:27]
	v_lshlrev_b32_e32 v32, 16, v4
	v_and_b32_e32 v33, 0xffff0000, v4
	v_lshlrev_b32_e32 v38, 16, v5
	v_and_b32_e32 v39, 0xffff0000, v5
	v_lshlrev_b32_e32 v18, 16, v12
	v_and_b32_e32 v19, 0xffff0000, v12
	v_lshlrev_b32_e32 v24, 16, v13
	v_and_b32_e32 v25, 0xffff0000, v13
	v_lshlrev_b32_e32 v4, 16, v47
	v_mov_b32_e32 v5, v10
	v_pk_mul_f32 v[2:3], v[14:15], v[14:15]
	v_and_b32_e32 v13, 0xffff0000, v48
	v_mov_b32_e32 v12, v9
	v_pk_mul_f32 v[56:57], v[32:33], v[32:33]
	v_pk_fma_f32 v[46:47], v[4:5], v[4:5], v[2:3]
	v_lshlrev_b32_e32 v6, 16, v48
	v_lshlrev_b32_e32 v2, 16, v49
	v_pk_mul_f32 v[48:49], v[12:13], v[12:13]
	v_add_f32_e32 v5, v54, v55
	v_add_f32_e32 v12, v52, v53
	v_pk_mul_f32 v[58:59], v[38:39], v[38:39]
	v_mov_b32_e32 v3, v6
	v_add_f32_e32 v5, v12, v5
	v_add_f32_e32 v12, v56, v57
	v_pk_mul_f32 v[60:61], v[18:19], v[18:19]
	v_pk_fma_f32 v[48:49], v[2:3], v[2:3], v[48:49]
	v_add_f32_e32 v3, v58, v59
	v_add_f32_e32 v5, v12, v5
	v_pk_mul_f32 v[62:63], v[24:25], v[24:25]
	v_add_f32_e32 v3, v3, v5
	v_add_f32_e32 v5, v60, v61
	v_pk_mul_f32 v[64:65], v[30:31], v[30:31]
	v_add_f32_e32 v3, v5, v3
	v_add_f32_e32 v5, v62, v63
	v_pk_mul_f32 v[70:71], v[36:37], v[36:37]
	v_lshlrev_b32_e32 v16, 16, v42
	v_and_b32_e32 v17, 0xffff0000, v42
	v_add_f32_e32 v3, v5, v3
	v_add_f32_e32 v5, v64, v65
	v_pk_mul_f32 v[72:73], v[16:17], v[16:17]
	v_lshlrev_b32_e32 v22, 16, v43
	v_and_b32_e32 v23, 0xffff0000, v43
	v_add_f32_e32 v3, v5, v3
	v_add_f32_e32 v5, v70, v71
	v_pk_mul_f32 v[42:43], v[22:23], v[22:23]
	v_lshlrev_b32_e32 v28, 16, v44
	v_and_b32_e32 v29, 0xffff0000, v44
	v_add_f32_e32 v3, v5, v3
	v_add_f32_e32 v5, v72, v73
	v_pk_mul_f32 v[74:75], v[28:29], v[28:29]
	v_lshlrev_b32_e32 v34, 16, v45
	v_and_b32_e32 v35, 0xffff0000, v45
	v_add_f32_e32 v3, v5, v3
	v_add_f32_e32 v5, v42, v43
	v_pk_mul_f32 v[44:45], v[34:35], v[34:35]
	v_add_f32_e32 v3, v5, v3
	v_add_f32_e32 v5, v74, v75
	v_add_f32_e32 v3, v5, v3
	v_add_f32_e32 v5, v44, v45
	v_add_f32_e32 v3, v5, v3
	v_and_b32_e32 v12, 64, v222
	v_add_f32_e32 v3, v47, v3
	v_xor_b32_e32 v5, 32, v222
	v_add_u32_e32 v12, 64, v12
	v_add_f32_e32 v3, v46, v3
	v_cmp_lt_i32_e32 vcc, v5, v12
	v_add_f32_e32 v3, v49, v3
	v_add_f32_e32 v3, v48, v3
	v_cndmask_b32_e32 v5, v222, v5, vcc
	v_lshlrev_b32_e32 v103, 2, v5
	ds_bpermute_b32 v5, v103, v3
	v_add_u32_e32 v42, s36, v76
	v_ashrrev_i32_e32 v43, 31, v42
	v_lshlrev_b64 v[42:43], 2, v[42:43]
	v_lshl_add_u64 v[42:43], s[58:59], 0, v[42:43]
	s_waitcnt lgkmcnt(0)
; #define LAS __attribute__((address_space(3)))
; __device__ __forceinline__ float bflo(unsigned w) { return __uint_as_float(w << 16); }
; __device__ __forceinline__ unsigned pkbf(float lo, float hi) { f32x2_t v = {lo, hi}; bf16x2_t b = __builtin_convertvector(v, bf16x2_t); return __builtin_bit_cast(unsigned, b); }
;     ...
;           const float snk = p.in[I_SINKS][l * 4 + hq] * LOG2E;
;           const float mref = fmaxf(sqrtf(qn2 * km2) * 1.001f * c2 + btab[hq * 132 + 131], snk);
;           u32x4 qxw; qxw.x = hi ? 0u : (pkbf(-mref, 0.f) & 0xffffu); qxw.y = 0u; qxw.z = 0u; qxw.w = 0u; qx = __builtin_bit_cast(bf16x8, qxw);
;           const float mrb = bflo(pkbf(-mref, 0.f));
;           lsum = hi == 0 ? __builtin_amdgcn_exp2f(snk + mrb) : 0.0f; }
;         f32x16 O[2];
; #pragma unroll
;         for (int d = 0; d < 2; ++d)
; #pragma unroll
;             for (int r = 0; r < 16; ++r) O[d][r] = 0.f;
;         const bf16_t* kbase = U + (size_t)b * LT * INW + C_KA + hkv * 64;
;         const bf16_t* vbase = VT + (size_t)bk * 64 * LTP;
;         const unsigned koff = (unsigned)(krow * INW + kch * 8), voff = (unsigned)(krow * LTP + kch * 8);
;         u32x4 kreg = *(const u32x4*)(kbase + koff), vreg = *(const u32x4*)(vbase + voff);
;         *(LAS u32x4*)(KV + krow * DF_PITCH + kch * 16) = kreg; *(LAS u32x4*)(KV + 2 * DF_KB + krow * DF_PITCH + kch * 16) = vreg;
;         __syncthreads();
	v_add_f32_e32 v3, v3, v5
	global_load_dword v5, v[42:43], off
	s_waitcnt vmcnt(1)
	v_mul_f32_e32 v0, v3, v0
	v_cmp_gt_f32_e32 vcc, s0, v0
	v_mul_f32_e32 v3, 0x4f800000, v0
	v_mul_hi_i32 v43, v104, s97
	v_cndmask_b32_e32 v0, v0, v3, vcc
	v_sqrt_f32_e32 v3, v0
	s_nop 0
	v_add_u32_e32 v12, -1, v3
	v_fma_f32 v14, -v12, v3, v0
	v_cmp_ge_f32_e64 s[0:1], 0, v14
	v_add_u32_e32 v14, 1, v3
	s_nop 0
	v_cndmask_b32_e64 v12, v3, v12, s[0:1]
	v_fma_f32 v3, -v14, v3, v0
	v_cmp_lt_f32_e64 s[0:1], 0, v3
	s_nop 1
	v_cndmask_b32_e64 v3, v12, v14, s[0:1]
	v_mul_f32_e32 v12, 0x37800000, v3
	v_cndmask_b32_e32 v3, v3, v12, vcc
	v_cmp_class_f32_e32 vcc, v0, v250
	s_movk_i32 s0, 0x210
	s_nop 0
	v_cndmask_b32_e32 v0, v3, v0, vcc
	v_mul_lo_u32 v3, v76, s0
	v_add_u32_e32 v122, 0, v3
	ds_read_b32 v3, v122 offset:524
	v_mul_f32_e32 v0, 0x3f8020c5, v0
	s_mov_b32 s0, 0x1616000
	v_mul_lo_u32 v42, v41, s0
	v_lshl_add_u64 v[42:43], s[16:17], 0, v[42:43]
	s_waitcnt lgkmcnt(0)
	v_fmac_f32_e32 v3, 0x3e38aa3b, v0
	s_mov_b32 s0, 0x41000
	s_waitcnt vmcnt(0)
	v_mul_f32_e32 v0, 0xbfb8aa3b, v5
	v_min_f32_e64 v0, -v3, v0
	v_cvt_pk_bf16_f32 v3, v0, 0
	v_lshlrev_b32_e32 v0, 16, v3
	v_fmac_f32_e32 v0, 0x3fb8aa3b, v5
	v_exp_f32_e32 v0, v0
	s_nop 0
	v_cndmask_b32_e64 v121, 0, v0, s[4:5]
	v_lshlrev_b32_e32 v0, 7, v11
	v_lshl_add_u64 v[108:109], v[42:43], 0, v[0:1]
	v_mul_lo_u32 v42, v8, s0
	v_ashrrev_i32_e32 v43, 31, v42
	v_lshlrev_b64 v[42:43], 1, v[42:43]
	v_lshl_add_u64 v[110:111], s[18:19], 0, v[42:43]
	v_lshl_add_u64 v[42:43], v[98:99], 1, v[108:109]
	global_load_dwordx4 v[70:73], v[42:43], off offset:512
	v_lshl_add_u64 v[42:43], v[100:101], 1, v[110:111]
	global_load_dwordx4 v[74:77], v[42:43], off
	v_readfirstlane_b32 s0, v51
	s_add_i32 s8, s37, -1
	s_min_i32 s9, s8, 1
	s_add_i32 s9, s9, s0
	s_add_i32 s9, s9, -1
	s_mul_i32 s30, s9, 0x2c000
	s_lshl_b32 s9, s9, 6
	v_add_u32_e32 v0, s30, v98
	v_lshl_add_u64 v[128:129], v[0:1], 1, v[108:109]
	global_load_dwordx4 v[136:139], v[128:129], off offset:512
	v_add_u32_e32 v0, s9, v100
	v_lshl_add_u64 v[128:129], v[0:1], 1, v[110:111]
	global_load_dwordx4 v[140:143], v[128:129], off
	s_min_i32 s9, s8, 2
	s_add_i32 s9, s9, s0
	s_add_i32 s9, s9, -1
	s_mul_i32 s30, s9, 0x2c000
	s_lshl_b32 s9, s9, 6
	v_add_u32_e32 v0, s30, v98
	v_lshl_add_u64 v[128:129], v[0:1], 1, v[108:109]
	global_load_dwordx4 v[144:147], v[128:129], off offset:512
	v_add_u32_e32 v0, s9, v100
	v_lshl_add_u64 v[128:129], v[0:1], 1, v[110:111]
	global_load_dwordx4 v[148:151], v[128:129], off
	s_min_i32 s9, s8, 3
	s_add_i32 s9, s9, s0
	s_add_i32 s9, s9, -1
	s_mul_i32 s30, s9, 0x2c000
	s_lshl_b32 s9, s9, 6
	v_add_u32_e32 v0, s30, v98
	v_lshl_add_u64 v[128:129], v[0:1], 1, v[108:109]
	global_load_dwordx4 v[196:199], v[128:129], off offset:512
	v_add_u32_e32 v0, s9, v100
	v_lshl_add_u64 v[128:129], v[0:1], 1, v[110:111]
	global_load_dwordx4 v[200:203], v[128:129], off
	s_min_i32 s9, s8, 4
	s_add_i32 s9, s9, s0
	s_add_i32 s9, s9, -1
	s_mul_i32 s30, s9, 0x2c000
	s_lshl_b32 s9, s9, 6
	v_add_u32_e32 v0, s30, v98
	v_lshl_add_u64 v[128:129], v[0:1], 1, v[108:109]
	global_load_dwordx4 v[206:209], v[128:129], off offset:512
	v_add_u32_e32 v0, s9, v100
	v_lshl_add_u64 v[128:129], v[0:1], 1, v[110:111]
	global_load_dwordx4 v[210:213], v[128:129], off
	s_min_i32 s9, s8, 5
	s_add_i32 s9, s9, s0
	s_add_i32 s9, s9, -1
	s_mul_i32 s30, s9, 0x2c000
	s_lshl_b32 s9, s9, 6
	v_add_u32_e32 v0, s30, v98
	v_lshl_add_u64 v[128:129], v[0:1], 1, v[108:109]
	global_load_dwordx4 v[232:235], v[128:129], off offset:512
	v_add_u32_e32 v0, s9, v100
	v_lshl_add_u64 v[128:129], v[0:1], 1, v[110:111]
	global_load_dwordx4 v[236:239], v[128:129], off
	v_add_u32_e32 v130, 0x9000, v113
	v_add_u32_e32 v131, 0x12000, v113
	s_waitcnt vmcnt(11)
	ds_write_b128 v113, v[70:73] offset:8192
	s_waitcnt vmcnt(10)
	ds_write_b128 v113, v[74:77] offset:26624
	s_waitcnt vmcnt(9)
	ds_write_b128 v113, v[136:139] offset:17408
	s_waitcnt vmcnt(8)
	ds_write_b128 v113, v[140:143] offset:35840
	s_waitcnt vmcnt(7)
	ds_write_b128 v130, v[144:147] offset:8192
	s_waitcnt vmcnt(6)
	ds_write_b128 v130, v[148:151] offset:26624
	s_waitcnt vmcnt(5)
	ds_write_b128 v130, v[196:199] offset:17408
	s_waitcnt vmcnt(4)
	ds_write_b128 v130, v[200:203] offset:35840
	s_waitcnt vmcnt(3)
	ds_write_b128 v131, v[206:209] offset:8192
	s_waitcnt vmcnt(2)
	ds_write_b128 v131, v[210:213] offset:26624
	s_waitcnt vmcnt(1)
	ds_write_b128 v131, v[232:235] offset:17408
	s_waitcnt vmcnt(0)
	ds_write_b128 v131, v[236:239] offset:35840
	s_waitcnt lgkmcnt(0)
	s_barrier
	s_cmp_lt_i32 s37, 1
	s_cbranch_scc1 .LBB0_819
	s_cmp_lg_u32 s37, 1
	s_mov_b32 s0, 0x2c000
	s_cselect_b64 s[30:31], -1, 0
	s_cmp_eq_u32 s37, 1
	v_mul_lo_u32 v52, v51, s0
	s_cbranch_scc1 .LBB0_817
	v_add_u32_e32 v0, v52, v98
	v_lshl_add_u64 v[42:43], v[0:1], 1, v[108:109]
	v_lshl_add_u32 v0, v51, 6, v100
	v_lshl_add_u64 v[44:45], v[0:1], 1, v[110:111]

; #define LAS __attribute__((address_space(3)))
;     ...
;         __syncthreads();
;         for (int ti = 0; ti < ntile; ++ti) {
;             const int kt = ti == 0 ? 0 : ktlo + ti - 1, k0 = kt * 64, cur = ti & 1;
;             if (ti + 1 < ntile) { const int kn = (ktlo + ti) * 64; kreg = *(const u32x4*)(kbase + (koff + (unsigned)(kn * INW))); vreg = *(const u32x4*)(vbase + (voff + (unsigned)kn)); }
;             if (wave_on && (kt == 0 || (k0 <= q0w + 31 && k0 + 63 >= q0w - 127)))
;                 swa_tile(KV + cur * DF_KB, KV + (2 + cur) * DF_KB, btab + hq * 132, Qf, qx, O, lsum, qpos, k0, l31, hi);
;             if (ti + 1 < ntile) { *(LAS u32x4*)(KV + (cur ^ 1) * DF_KB + krow * DF_PITCH + kch * 16) = kreg; *(LAS u32x4*)(KV + (2 + (cur ^ 1)) * DF_KB + krow * DF_PITCH + kch * 16) = vreg; }
.LBB0_821:
.LBB0_822:
	s_and_b64 vcc, exec, s[0:1]
	s_waitcnt lgkmcnt(0)
	s_barrier
	s_cbranch_vccnz .LBB0_833
	v_lshlrev_b32_e32 v125, 6, v51
	v_add_u32_e32 v34, v119, v50
	v_add_u32_e32 v123, 31, v120
	v_add_u32_e32 v124, 0xffffff81, v120
	v_add_u32_e32 v0, v117, v52
	v_sub_u32_e32 v126, v34, v125
	s_mov_b32 s0, 1

; #define LAS __attribute__((address_space(3)))
; __device__ __forceinline__ void swa_tile(const LAS unsigned char* Kb, const LAS unsigned char* Vb, const LAS float* btab, const bf16x8 (&Qf)[4], const bf16x8 qx, f32x16 (&O)[2],
;                                          float& lsum, int qpos, int k0, int l31, int hi) {
;     ...
;     f32x16 S[2];
; #pragma unroll
;     for (int kb = 0; kb < 2; ++kb) {
;         f32x16 acc;
; #pragma unroll
;         for (int r = 0; r < 16; ++r) acc[r] = 0.f;
; #pragma unroll
;         for (int s = 0; s < 4; ++s) { const bf16x8 kf = *(const LAS bf16x8*)(Kb + (32 * kb + l31) * DF_PITCH + s * 32 + hi * 16);
;             acc = __builtin_amdgcn_mfma_f32_32x32x16_bf16(kf, Qf[s], acc, 0, 0, 0); }
;         acc = __builtin_amdgcn_mfma_f32_32x32x16_bf16(kx, qx, acc, 0, 0, 0);
;         S[kb] = acc;
;     }
;     float ls = 0.f;
;     bf16x8 Pf[4];
; #pragma unroll
;     for (int kb = 0; kb < 2; ++kb) {
; #pragma unroll
;         for (int r = 0; r < 16; ++r) { const int j = k0 + 32 * kb + (r & 3) + 8 * (r >> 2) + 4 * hi, dist = qpos - j;
;             const LAS float* tb = (k0 == 0 && kb == 0 && r < 8) ? btab + 4 * 132 : btab;
;             const float pv = __builtin_amdgcn_exp2f(S[kb][r] + tb[min(max(dist + 1, 0), 129)]); ls += pv; S[kb][r] = pv; }
;     ...
;         for (int ti = 0; ti < ntile; ++ti) {
;             const int kt = ti == 0 ? 0 : ktlo + ti - 1, k0 = kt * 64, cur = ti & 1;
;             if (ti + 1 < ntile) { const int kn = (ktlo + ti) * 64; kreg = *(const u32x4*)(kbase + (koff + (unsigned)(kn * INW))); vreg = *(const u32x4*)(vbase + (voff + (unsigned)kn)); }
;             if (wave_on && (kt == 0 || (k0 <= q0w + 31 && k0 + 63 >= q0w - 127)))
;                 swa_tile(KV + cur * DF_KB, KV + (2 + cur) * DF_KB, btab + hq * 132, Qf, qx, O, lsum, qpos, k0, l31, hi);
.LBB0_826:
	s_and_b64 vcc, exec, s[8:9]
	s_and_b32 s39, s0, 1
	s_cbranch_vccnz .LBB0_829
	v_add_u32_e32 v34, 63, v125
	v_cmp_gt_i32_e32 vcc, v125, v123
	v_cmp_lt_i32_e64 s[0:1], v34, v124
	s_or_b64 s[0:1], vcc, s[0:1]
	s_and_b64 vcc, exec, s[0:1]
	s_cbranch_vccnz .LBB0_829
	s_add_i32 s0, s38, -1
	s_lshr_b32 s0, s0, 1
	s_mul_i32 s0, s0, 0x9000
	s_mul_i32 s1, s39, 0x2400
	s_add_i32 s0, s0, s1
	v_add_u32_e32 v127, s0, v115
	ds_read_b128 v[136:139], v127 offset:8192
	ds_read_b128 v[140:143], v127 offset:8224
	ds_read_b128 v[144:147], v127 offset:8256
	ds_read_b128 v[148:151], v127 offset:8288
	ds_read_b128 v[196:199], v127 offset:12800
	ds_read_b128 v[200:203], v127 offset:12832
	ds_read_b128 v[206:209], v127 offset:12864
	ds_read_b128 v[210:213], v127 offset:12896
	v_add_u32_e32 v184, 59, v126
	v_max_i32_e32 v184, -1, v184
	v_add_u32_e32 v184, 1, v184
	v_min_u32_e32 v184, 0x81, v184
	v_lshl_add_u32 v184, v184, 2, v122
	ds_read_b32 v184, v184
	v_add_u32_e32 v185, 58, v126
	v_max_i32_e32 v185, -1, v185
	v_add_u32_e32 v185, 1, v185
	v_min_u32_e32 v185, 0x81, v185
	v_lshl_add_u32 v185, v185, 2, v122
	ds_read_b32 v185, v185
	v_add_u32_e32 v186, 57, v126
	v_max_i32_e32 v186, -1, v186
	v_add_u32_e32 v186, 1, v186
	v_min_u32_e32 v186, 0x81, v186
	v_lshl_add_u32 v186, v186, 2, v122
	ds_read_b32 v186, v186
	v_add_u32_e32 v187, 56, v126
	v_max_i32_e32 v187, -1, v187
	v_add_u32_e32 v187, 1, v187
	v_min_u32_e32 v187, 0x81, v187
	v_lshl_add_u32 v187, v187, 2, v122
	ds_read_b32 v187, v187
	s_waitcnt lgkmcnt(11)
	v_mfma_f32_32x32x16_bf16 v[50:65], v[136:139], v[82:85], 0
	v_add_u32_e32 v188, 51, v126
	v_max_i32_e32 v188, -1, v188
	v_add_u32_e32 v188, 1, v188
	v_min_u32_e32 v188, 0x81, v188
	v_lshl_add_u32 v188, v188, 2, v122
	ds_read_b32 v188, v188
	s_waitcnt lgkmcnt(11)
	v_mfma_f32_32x32x16_bf16 v[50:65], v[140:143], v[86:89], v[50:65]
	v_add_u32_e32 v189, 50, v126
	v_max_i32_e32 v189, -1, v189
	v_add_u32_e32 v189, 1, v189
	v_min_u32_e32 v189, 0x81, v189
	v_lshl_add_u32 v189, v189, 2, v122
	ds_read_b32 v189, v189
	s_waitcnt lgkmcnt(11)
	v_mfma_f32_32x32x16_bf16 v[50:65], v[144:147], v[90:93], v[50:65]
	v_add_u32_e32 v194, 49, v126
	v_max_i32_e32 v194, -1, v194
	v_add_u32_e32 v194, 1, v194
	v_min_u32_e32 v194, 0x81, v194
	v_lshl_add_u32 v194, v194, 2, v122
	ds_read_b32 v194, v194
	s_waitcnt lgkmcnt(11)
	v_mfma_f32_32x32x16_bf16 v[50:65], v[148:151], v[94:97], v[50:65]
	v_add_u32_e32 v195, 48, v126
	v_max_i32_e32 v195, -1, v195
	v_add_u32_e32 v195, 1, v195
	v_min_u32_e32 v195, 0x81, v195
	v_lshl_add_u32 v195, v195, 2, v122
	ds_read_b32 v195, v195
	s_waitcnt lgkmcnt(11)
	v_mfma_f32_32x32x16_bf16 v[34:49], v[196:199], v[82:85], 0
	v_add_u32_e32 v229, 43, v126
	v_max_i32_e32 v229, -1, v229
	v_add_u32_e32 v229, 1, v229
	v_min_u32_e32 v229, 0x81, v229
	v_lshl_add_u32 v229, v229, 2, v122
	ds_read_b32 v229, v229
	s_waitcnt lgkmcnt(11)
	v_mfma_f32_32x32x16_bf16 v[34:49], v[200:203], v[86:89], v[34:49]
	v_add_u32_e32 v230, 42, v126
	v_max_i32_e32 v230, -1, v230
	v_add_u32_e32 v230, 1, v230
	v_min_u32_e32 v230, 0x81, v230
	v_lshl_add_u32 v230, v230, 2, v122
	ds_read_b32 v230, v230
	s_waitcnt lgkmcnt(11)
	v_mfma_f32_32x32x16_bf16 v[34:49], v[206:209], v[90:93], v[34:49]
	v_add_u32_e32 v231, 41, v126
	v_max_i32_e32 v231, -1, v231
	v_add_u32_e32 v231, 1, v231
	v_min_u32_e32 v231, 0x81, v231
	v_lshl_add_u32 v231, v231, 2, v122
	ds_read_b32 v231, v231
	s_waitcnt lgkmcnt(11)
	v_mfma_f32_32x32x16_bf16 v[34:49], v[210:213], v[94:97], v[34:49]
	v_add_u32_e32 v248, 40, v126
	v_max_i32_e32 v248, -1, v248
	v_add_u32_e32 v248, 1, v248
	v_min_u32_e32 v248, 0x81, v248
	v_lshl_add_u32 v248, v248, 2, v122
	ds_read_b32 v248, v248
	v_mfma_f32_32x32x16_bf16 v[50:65], v[66:69], v[78:81], v[50:65]
	v_mfma_f32_32x32x16_bf16 v[34:49], v[66:69], v[78:81], v[34:49]
	s_nop 9
	s_waitcnt lgkmcnt(11)
	v_add_f32_e32 v50, v50, v184
	v_add_u32_e32 v184, 35, v126
	v_max_i32_e32 v184, -1, v184
	v_add_u32_e32 v184, 1, v184
	v_min_u32_e32 v184, 0x81, v184
	v_lshl_add_u32 v184, v184, 2, v122
	ds_read_b32 v184, v184
	v_exp_f32_e32 v128, v50
	s_waitcnt lgkmcnt(11)
	v_add_f32_e32 v50, v51, v185
	v_add_u32_e32 v185, 34, v126
	v_max_i32_e32 v185, -1, v185
	v_add_u32_e32 v185, 1, v185
	v_min_u32_e32 v185, 0x81, v185
	v_lshl_add_u32 v185, v185, 2, v122
	ds_read_b32 v185, v185
	v_exp_f32_e32 v129, v50
	s_waitcnt lgkmcnt(11)
	v_add_f32_e32 v50, v52, v186
	v_add_u32_e32 v186, 33, v126
	v_max_i32_e32 v186, -1, v186
	v_add_u32_e32 v186, 1, v186
	v_min_u32_e32 v186, 0x81, v186
	v_lshl_add_u32 v186, v186, 2, v122
	ds_read_b32 v186, v186
	v_exp_f32_e32 v130, v50
	s_waitcnt lgkmcnt(11)
	v_add_f32_e32 v50, v53, v187
	v_add_u32_e32 v187, 32, v126
	v_max_i32_e32 v187, -1, v187
	v_add_u32_e32 v187, 1, v187
	v_min_u32_e32 v187, 0x81, v187
	v_lshl_add_u32 v187, v187, 2, v122
	ds_read_b32 v187, v187
	v_exp_f32_e32 v131, v50
	s_waitcnt lgkmcnt(11)
	v_add_f32_e32 v50, v54, v188
	v_add_u32_e32 v188, 27, v126
	v_max_i32_e32 v188, -1, v188
	v_add_u32_e32 v188, 1, v188
	v_min_u32_e32 v188, 0x81, v188
	v_lshl_add_u32 v188, v188, 2, v122
	ds_read_b32 v188, v188
	v_exp_f32_e32 v132, v50
	v_cvt_pk_bf16_f32 v54, v128, v129
	v_add_f32_e32 v128, 0, v128
	v_add_f32_e32 v128, v128, v129
	v_add_f32_e32 v128, v128, v130
	s_waitcnt lgkmcnt(11)
	v_add_f32_e32 v50, v55, v189
	v_add_u32_e32 v189, 26, v126
	v_max_i32_e32 v189, -1, v189
	v_add_u32_e32 v189, 1, v189
	v_min_u32_e32 v189, 0x81, v189
	v_lshl_add_u32 v189, v189, 2, v122
	ds_read_b32 v189, v189
	v_exp_f32_e32 v133, v50
	v_add_f32_e32 v128, v128, v131
	v_add_f32_e32 v128, v128, v132
	v_add_f32_e32 v128, v128, v133
	v_cvt_pk_bf16_f32 v55, v130, v131
	s_waitcnt lgkmcnt(11)
; #define LAS __attribute__((address_space(3)))
; __device__ __forceinline__ void swa_tile(const LAS unsigned char* Kb, const LAS unsigned char* Vb, const LAS float* btab, const bf16x8 (&Qf)[4], const bf16x8 qx, f32x16 (&O)[2],
;                                          float& lsum, int qpos, int k0, int l31, int hi) {
;     ...
;     float ls = 0.f;
;     bf16x8 Pf[4];
; #pragma unroll
;     for (int kb = 0; kb < 2; ++kb) {
; #pragma unroll
;         for (int r = 0; r < 16; ++r) { const int j = k0 + 32 * kb + (r & 3) + 8 * (r >> 2) + 4 * hi, dist = qpos - j;
;             const LAS float* tb = (k0 == 0 && kb == 0 && r < 8) ? btab + 4 * 132 : btab;
;             const float pv = __builtin_amdgcn_exp2f(S[kb][r] + tb[min(max(dist + 1, 0), 129)]); ls += pv; S[kb][r] = pv; }
; #pragma unroll
;         for (int s = 0; s < 2; ++s) Pf[2 * kb + s] = pack_acc(S[kb], s);
;     }
;     lsum += ls;
; #pragma unroll
;     for (int st = 0; st < 4; ++st) { asm volatile("" ::: "memory");
; #pragma unroll
;         for (int dvb = 0; dvb < 2; ++dvb) { const bf16x8 vf = *(const LAS bf16x8*)(Vb + (32 * dvb + l31) * DF_PITCH + st * 32 + hi * 16);
;             O[dvb] = __builtin_amdgcn_mfma_f32_32x32x16_bf16(vf, Pf[st], O[dvb], 0, 0, 0); } }
;     asm volatile("" ::: "memory");
	v_add_f32_e32 v50, v56, v194
	v_add_u32_e32 v194, 25, v126
	v_max_i32_e32 v194, -1, v194
	v_add_u32_e32 v194, 1, v194
	v_min_u32_e32 v194, 0x81, v194
	v_lshl_add_u32 v194, v194, 2, v122
	ds_read_b32 v194, v194
	v_exp_f32_e32 v134, v50
	s_nop 0
	v_add_f32_e32 v128, v128, v134
	v_cvt_pk_bf16_f32 v56, v132, v133
	s_waitcnt lgkmcnt(11)
	v_add_f32_e32 v50, v57, v195
	v_add_u32_e32 v195, 24, v126
	v_max_i32_e32 v195, -1, v195
	v_add_u32_e32 v195, 1, v195
	v_min_u32_e32 v195, 0x81, v195
	v_lshl_add_u32 v195, v195, 2, v122
	ds_read_b32 v195, v195
	v_exp_f32_e32 v135, v50
	s_nop 0
	v_add_f32_e32 v128, v128, v135
	v_cvt_pk_bf16_f32 v57, v134, v135
	s_waitcnt lgkmcnt(11)
	v_add_f32_e32 v50, v58, v229
	v_add_u32_e32 v229, 19, v126
	v_max_i32_e32 v229, -1, v229
	v_add_u32_e32 v229, 1, v229
	v_min_u32_e32 v229, 0x81, v229
	v_lshl_add_u32 v229, v229, 2, v122
	ds_read_b32 v229, v229
	v_exp_f32_e32 v58, v50
	s_waitcnt lgkmcnt(11)
	v_add_f32_e32 v50, v59, v230
	v_add_u32_e32 v230, 18, v126
	v_max_i32_e32 v230, -1, v230
	v_add_u32_e32 v230, 1, v230
	v_min_u32_e32 v230, 0x81, v230
	v_lshl_add_u32 v230, v230, 2, v122
	ds_read_b32 v230, v230
	v_exp_f32_e32 v59, v50
	s_waitcnt lgkmcnt(11)
	v_add_f32_e32 v50, v60, v231
	v_add_u32_e32 v231, 17, v126
	v_max_i32_e32 v231, -1, v231
	v_add_u32_e32 v231, 1, v231
	v_min_u32_e32 v231, 0x81, v231
	v_lshl_add_u32 v231, v231, 2, v122
	ds_read_b32 v231, v231
	v_exp_f32_e32 v60, v50
	s_waitcnt lgkmcnt(11)
	v_add_f32_e32 v50, v61, v248
	v_add_u32_e32 v248, 16, v126
	v_max_i32_e32 v248, -1, v248
	v_add_u32_e32 v248, 1, v248
	v_min_u32_e32 v248, 0x81, v248
	v_lshl_add_u32 v248, v248, 2, v122
	ds_read_b32 v248, v248
	v_exp_f32_e32 v61, v50
	s_nop 0
	v_cvt_pk_bf16_f32 v51, v60, v61
	s_waitcnt lgkmcnt(11)
	v_add_f32_e32 v50, v62, v184
	v_add_u32_e32 v184, 11, v126
	v_max_i32_e32 v184, -1, v184
	v_add_u32_e32 v184, 1, v184
	v_min_u32_e32 v184, 0x81, v184
	v_lshl_add_u32 v184, v184, 2, v122
	ds_read_b32 v184, v184
	v_exp_f32_e32 v62, v50
	s_waitcnt lgkmcnt(11)
	v_add_f32_e32 v50, v63, v185
	v_add_u32_e32 v185, 10, v126
	v_max_i32_e32 v185, -1, v185
	v_add_u32_e32 v185, 1, v185
	v_min_u32_e32 v185, 0x81, v185
	v_lshl_add_u32 v185, v185, 2, v122
	ds_read_b32 v185, v185
	v_exp_f32_e32 v63, v50
	s_nop 0
	v_cvt_pk_bf16_f32 v52, v62, v63
	s_waitcnt lgkmcnt(11)
	v_add_f32_e32 v50, v64, v186
	v_add_u32_e32 v186, 9, v126
	v_max_i32_e32 v186, -1, v186
	v_add_u32_e32 v186, 1, v186
	v_min_u32_e32 v186, 0x81, v186
	v_lshl_add_u32 v186, v186, 2, v122
	ds_read_b32 v186, v186
	v_exp_f32_e32 v64, v50
	s_waitcnt lgkmcnt(11)
	v_add_f32_e32 v50, v65, v187
	v_add_u32_e32 v187, 8, v126
	v_max_i32_e32 v187, -1, v187
	v_add_u32_e32 v187, 1, v187
	v_min_u32_e32 v187, 0x81, v187
	v_lshl_add_u32 v187, v187, 2, v122
	ds_read_b32 v187, v187
	v_exp_f32_e32 v65, v50
	v_cvt_pk_bf16_f32 v50, v58, v59
	v_add_f32_e32 v58, v128, v58
	v_add_f32_e32 v58, v58, v59
	v_add_f32_e32 v58, v58, v60
	v_add_f32_e32 v58, v58, v61
	v_add_f32_e32 v58, v58, v62
	v_add_f32_e32 v58, v58, v63
	s_waitcnt lgkmcnt(11)
	v_add_f32_e32 v34, v34, v188
	v_add_u32_e32 v188, 3, v126
	v_max_i32_e32 v188, -1, v188
	v_add_u32_e32 v188, 1, v188
	v_min_u32_e32 v188, 0x81, v188
	v_lshl_add_u32 v188, v188, 2, v122
	ds_read_b32 v188, v188
	v_exp_f32_e32 v59, v34
	v_cvt_pk_bf16_f32 v53, v64, v65
	v_add_f32_e32 v58, v58, v64
	v_add_f32_e32 v58, v58, v65
	v_add_f32_e32 v58, v58, v59
	s_waitcnt lgkmcnt(11)
	v_add_f32_e32 v34, v35, v189
	v_add_u32_e32 v189, 2, v126
	v_max_i32_e32 v189, -1, v189
	v_add_u32_e32 v189, 1, v189
	v_min_u32_e32 v189, 0x81, v189
	v_lshl_add_u32 v189, v189, 2, v122
	ds_read_b32 v189, v189
	v_exp_f32_e32 v60, v34
	s_nop 0
	v_add_f32_e32 v58, v58, v60
	s_waitcnt lgkmcnt(11)
	v_add_f32_e32 v34, v36, v194
	v_add_u32_e32 v194, 1, v126
	v_max_i32_e32 v194, -1, v194
	v_add_u32_e32 v194, 1, v194
	v_min_u32_e32 v194, 0x81, v194
	v_lshl_add_u32 v194, v194, 2, v122
	ds_read_b32 v194, v194
	v_exp_f32_e32 v61, v34
	s_nop 0
	v_add_f32_e32 v58, v58, v61
	s_waitcnt lgkmcnt(11)
	v_add_f32_e32 v34, v37, v195
	v_max_i32_e32 v195, -1, v126
	v_add_u32_e32 v195, 1, v195
	v_min_u32_e32 v195, 0x81, v195
	v_lshl_add_u32 v195, v195, 2, v122
	ds_read_b32 v195, v195
	v_exp_f32_e32 v62, v34
	s_nop 0
	v_add_f32_e32 v58, v58, v62
	s_waitcnt lgkmcnt(11)
	v_add_f32_e32 v34, v38, v229
	ds_read_b128 v[232:235], v127 offset:26624
	v_exp_f32_e32 v63, v34
	s_nop 0
	v_add_f32_e32 v58, v58, v63
	v_cvt_pk_bf16_f32 v38, v59, v60
	s_waitcnt lgkmcnt(11)
	v_add_f32_e32 v34, v39, v230
	ds_read_b128 v[236:239], v127 offset:31232
	v_exp_f32_e32 v64, v34
	s_nop 0
	v_add_f32_e32 v58, v58, v64
	v_cvt_pk_bf16_f32 v39, v61, v62
	s_waitcnt lgkmcnt(11)
	v_add_f32_e32 v34, v40, v231
	ds_read_b128 v[240:243], v127 offset:26656
	v_exp_f32_e32 v65, v34
	s_nop 0
	v_add_f32_e32 v58, v58, v65
	v_cvt_pk_bf16_f32 v40, v63, v64
	s_waitcnt lgkmcnt(11)
	v_add_f32_e32 v34, v41, v248
	ds_read_b128 v[244:247], v127 offset:31264
	v_exp_f32_e32 v128, v34
	s_nop 0
	v_add_f32_e32 v58, v58, v128
	v_cvt_pk_bf16_f32 v41, v65, v128
	s_waitcnt lgkmcnt(11)
	v_add_f32_e32 v34, v42, v184
	ds_read_b128 v[136:139], v127 offset:26688
	v_exp_f32_e32 v42, v34
	s_waitcnt lgkmcnt(11)
	v_add_f32_e32 v34, v43, v185
	ds_read_b128 v[140:143], v127 offset:31296
	v_exp_f32_e32 v43, v34
	s_waitcnt lgkmcnt(11)
	v_add_f32_e32 v34, v44, v186
	ds_read_b128 v[144:147], v127 offset:26720
	v_exp_f32_e32 v44, v34
	s_waitcnt lgkmcnt(11)
	v_add_f32_e32 v34, v45, v187
	ds_read_b128 v[148:151], v127 offset:31328
	v_exp_f32_e32 v45, v34
	s_nop 0
	v_cvt_pk_bf16_f32 v35, v44, v45
	s_waitcnt lgkmcnt(11)
	v_add_f32_e32 v34, v46, v188
	v_exp_f32_e32 v46, v34
	s_waitcnt lgkmcnt(10)
	v_add_f32_e32 v34, v47, v189
	v_exp_f32_e32 v47, v34
	s_nop 0
	v_cvt_pk_bf16_f32 v36, v46, v47
	s_waitcnt lgkmcnt(9)
	v_add_f32_e32 v34, v48, v194
	v_exp_f32_e32 v48, v34
	s_waitcnt lgkmcnt(8)
	v_add_f32_e32 v34, v49, v195
	v_exp_f32_e32 v49, v34
	v_cvt_pk_bf16_f32 v34, v42, v43
	v_add_f32_e32 v42, v58, v42
	v_add_f32_e32 v42, v42, v43
	v_add_f32_e32 v42, v42, v44
	v_add_f32_e32 v42, v42, v45
	v_add_f32_e32 v42, v42, v46
	v_add_f32_e32 v42, v42, v47
	v_add_f32_e32 v42, v42, v48
	v_add_f32_e32 v42, v42, v49
	v_add_f32_e32 v121, v121, v42
	s_waitcnt lgkmcnt(7)
	v_mfma_f32_32x32x16_bf16 v[18:33], v[232:235], v[54:57], v[18:33]
	v_cvt_pk_bf16_f32 v37, v48, v49
	s_waitcnt lgkmcnt(6)
	v_mfma_f32_32x32x16_bf16 v[2:17], v[236:239], v[54:57], v[2:17]
	s_waitcnt lgkmcnt(5)
	v_mfma_f32_32x32x16_bf16 v[18:33], v[240:243], v[50:53], v[18:33]
	s_waitcnt lgkmcnt(4)
	v_mfma_f32_32x32x16_bf16 v[2:17], v[244:247], v[50:53], v[2:17]
	s_waitcnt lgkmcnt(3)
	v_mfma_f32_32x32x16_bf16 v[18:33], v[136:139], v[38:41], v[18:33]
	s_waitcnt lgkmcnt(2)
	v_mfma_f32_32x32x16_bf16 v[2:17], v[140:143], v[38:41], v[2:17]
	s_waitcnt lgkmcnt(1)
	v_mfma_f32_32x32x16_bf16 v[18:33], v[144:147], v[34:37], v[18:33]
	s_waitcnt lgkmcnt(0)
	v_mfma_f32_32x32x16_bf16 v[2:17], v[148:151], v[34:37], v[2:17]
; #define LAS __attribute__((address_space(3)))
;     ...
;             if (ti + 1 < ntile) { *(LAS u32x4*)(KV + (cur ^ 1) * DF_KB + krow * DF_PITCH + kch * 16) = kreg; *(LAS u32x4*)(KV + (2 + (cur ^ 1)) * DF_KB + krow * DF_PITCH + kch * 16) = vreg; }
;             __syncthreads();
;         }
.LBB0_829:
	s_andn2_b64 vcc, exec, s[30:31]
	s_cbranch_vccnz .LBB0_831
.LBB0_831:
	v_add_u32_e32 v0, 0x2c000, v0
	v_add_u32_e32 v125, 64, v125
	s_cmp_eq_u32 s37, s38
	v_subrev_u32_e32 v126, 64, v126
	s_waitcnt lgkmcnt(0)
	s_barrier
	s_cbranch_scc1 .LBB0_833
	s_mov_b32 s0, s38
	s_branch .LBB0_824
